# conversion loads of a continued slice: scalar base advanced by SALU + four fixed per-lane 32-bit offsets (no per-iteration 64-bit address rebuild)
# baseline (speedup 1.0000x reference)
; DEVI f32x4 ld_nt(const float* p) { return __builtin_nontemporal_load((const f32x4*)p); }
; DEVI void cv_next(const Params& p, int l, int s, int lane, int stride, CvRun& run) {
;     ...
;     run.c = cv_slice(p, l, s, lane); run.left = 0;
;     if ((stride & 511) == 0) {
;         if (s < NS_W13) { const int e = s >> 9, es = stride >> 9; if (e < NE) { run.left = (NE - 1 - e) / es; run.sstep = (long)es * 1024 * 256; run.dstep = (long)es * 512 * 1024; } }
;         else { const int e = (s - NS_W13) >> 8, es = stride >> 8; if (e < NE) { run.left = (NE - 1 - e) / es; run.sstep = (long)es * 256 * 1024; run.dstep = (long)es * 1024 * 256; } } }
; }
; DEVI void cv_issue(const Params& p, int l, int s, int lane, CvRegs& R, CvRun& run) {
;     R.live = s < NS_SLICES ? 1 : 0;
;     if (R.live) { cv_next(p, l, s, lane, (int)gridDim.x * 8, run); R.c = run.c; const int kq = lane >> 3;
;         const float* sp = R.c.src + (size_t)(R.c.k0 + 2 * kq) * R.c.ld;
;         R.a0 = ld_nt(sp); R.b0 = ld_nt(sp + R.c.ld); R.a1 = ld_nt(sp + (size_t)16 * R.c.ld); R.b1 = ld_nt(sp + (size_t)17 * R.c.ld); }
.LBB0_693:
	s_and_b64 vcc, exec, s[16:17]
	s_cbranch_vccz .LBB0_695
	s_lshl_b64 s[6:7], s[26:27], 1
	s_lshl_b64 s[16:17], s[28:29], 2
	s_add_u32 s68, s68, s16
	s_addc_u32 s69, s69, s17
	v_lshl_add_u64 v[172:173], v[172:173], 0, s[6:7]
	s_add_i32 s56, s56, -1
	s_mov_b32 s8, s60
	s_mov_b32 s94, s59
	s_mov_b32 s10, s58
	s_mov_b32 s95, s55
	s_mov_b32 s6, s57
	global_load_dwordx4 v[154:157], v242, s[68:69] nt
	global_load_dwordx4 v[158:161], v243, s[68:69] nt
	global_load_dwordx4 v[162:165], v244, s[68:69] nt
	global_load_dwordx4 v[166:169], v245, s[68:69] nt
	s_branch .LBB0_696


; DEVI f32x4 ld_nt(const float* p) { return __builtin_nontemporal_load((const f32x4*)p); }
; DEVI void cv_next(const Params& p, int l, int s, int lane, int stride, CvRun& run) {
;     ...
;     run.c = cv_slice(p, l, s, lane); run.left = 0;
;     if ((stride & 511) == 0) {
;         if (s < NS_W13) { const int e = s >> 9, es = stride >> 9; if (e < NE) { run.left = (NE - 1 - e) / es; run.sstep = (long)es * 1024 * 256; run.dstep = (long)es * 512 * 1024; } }
;         else { const int e = (s - NS_W13) >> 8, es = stride >> 8; if (e < NE) { run.left = (NE - 1 - e) / es; run.sstep = (long)es * 256 * 1024; run.dstep = (long)es * 1024 * 256; } } }
; }
; DEVI void cv_issue(const Params& p, int l, int s, int lane, CvRegs& R, CvRun& run) {
;     R.live = s < NS_SLICES ? 1 : 0;
;     if (R.live) { cv_next(p, l, s, lane, (int)gridDim.x * 8, run); R.c = run.c; const int kq = lane >> 3;
;         const float* sp = R.c.src + (size_t)(R.c.k0 + 2 * kq) * R.c.ld;
;         R.a0 = ld_nt(sp); R.b0 = ld_nt(sp + R.c.ld); R.a1 = ld_nt(sp + (size_t)16 * R.c.ld); R.b1 = ld_nt(sp + (size_t)17 * R.c.ld); }
.LBB0_695:
	v_add_u32_e32 v252, s10, v128
	s_mov_b64 s[68:69], s[18:19]
	v_mul_lo_u32 v243, v252, s6
	v_lshlrev_b32_e32 v242, 2, v114
	s_lshl_b32 s72, s6, 2
	s_lshl_b32 s73, s6, 6
	v_lshl_add_u32 v242, v243, 2, v242
	v_add_u32_e32 v243, s72, v242
	v_add_u32_e32 v244, s73, v242
	v_add_u32_e32 v245, s73, v243
	s_ashr_i32 s7, s6, 31
	v_mad_i64_i32 v[252:253], s[16:17], v252, s6, 0
	v_lshl_add_u64 v[252:253], v[252:253], 2, v[250:251]
	s_lshl_b64 s[16:17], s[6:7], 2
	v_lshl_add_u64 v[254:255], v[252:253], 0, s[16:17]
	global_load_dwordx4 v[154:157], v[252:253], off nt
	global_load_dwordx4 v[158:161], v[254:255], off nt
	v_mad_i64_i32 v[252:253], s[18:19], s6, 60, v[254:255]
	v_lshl_add_u64 v[254:255], v[252:253], 0, s[16:17]
	global_load_dwordx4 v[162:165], v[252:253], off nt
	global_load_dwordx4 v[166:169], v[254:255], off nt
	s_mov_b64 s[26:27], s[22:23]
	s_mov_b64 s[28:29], s[50:51]
	s_mov_b32 s56, s11
	s_mov_b32 s55, s95
	v_mov_b64_e32 v[170:171], v[250:251]
	s_mov_b32 s57, s6
	s_mov_b32 s58, s10
	v_mov_b64_e32 v[172:173], v[182:183]
	s_mov_b32 s59, s94
	s_mov_b32 s60, s8

; DEVI CvSlice cv_slice(const Params& p, int l, int s, int lane) {
;     CvSlice c;
;     if (s < NS_W13) {
;         const int e = s >> 9, r = s & 511, hb = r & 7, mat = (r >> 3) & 1, ks = r >> 4;
;         const float* W = mat ? (e < NE ? p.w3 + ((size_t)l * NE + e) * 1024 * 256 : p.ws3 + (size_t)l * 1024 * 256)
;                              : (e < NE ? p.w1 + ((size_t)l * NE + e) * 1024 * 256 : p.ws1 + (size_t)l * 1024 * 256);
;         const int hc0 = hb * 32;
;         c.src = W + hc0 + (lane & 7) * 4; c.ld = 256; c.dst = p.w13t + (size_t)e * 512 * 1024; c.K = 1024;
;         c.r0 = (hc0 >> 7) * 256 + ((hc0 >> 5) & 3) * 32 + mat * 16; c.k0 = ks * 32; c.perm = 0;
;     } else {
;         s -= NS_W13;
;         const int e = s >> 8, r = s & 255, nb = r & 31, ks = r >> 5;
;         const float* W2 = e < NE ? p.w2 + ((size_t)l * NE + e) * 256 * 1024 : p.ws2 + (size_t)l * 256 * 1024;
;         c.src = W2 + nb * 32 + (lane & 7) * 4; c.ld = 1024; c.dst = p.w2t + (size_t)e * 1024 * 256; c.K = 256; c.r0 = (nb >> 3) * 256 + ((nb & 7) >> 1) * 32 + (nb & 1) * 8; c.k0 = ks * 32; c.perm = 1;
;     }
;     return c;
; }
; DEVI void cv_next(const Params& p, int l, int s, int lane, int stride, CvRun& run) {
;     ...
;     run.c = cv_slice(p, l, s, lane); run.left = 0;
;     if ((stride & 511) == 0) {
;         if (s < NS_W13) { const int e = s >> 9, es = stride >> 9; if (e < NE) { run.left = (NE - 1 - e) / es; run.sstep = (long)es * 1024 * 256; run.dstep = (long)es * 512 * 1024; } }
;         else { const int e = (s - NS_W13) >> 8, es = stride >> 8; if (e < NE) { run.left = (NE - 1 - e) / es; run.sstep = (long)es * 256 * 1024; run.dstep = (long)es * 1024 * 256; } } }
; }
; DEVI void cv_issue(const Params& p, int l, int s, int lane, CvRegs& R, CvRun& run) {
;     R.live = s < NS_SLICES ? 1 : 0;
;     if (R.live) { cv_next(p, l, s, lane, (int)gridDim.x * 8, run); R.c = run.c; const int kq = lane >> 3;
.LBB0_718:
	v_lshlrev_b32_e32 v250, 2, v114
	v_mov_b32_e32 v251, 0
	v_lshl_add_u64 v[170:171], s[68:69], 0, v[250:251]
	s_cmp_lt_i32 s54, 0x30300
	s_cselect_b64 s[12:13], -1, 0
	s_cmp_gt_i32 s54, 0x302ff
	s_cbranch_scc1 .LBB0_748
	s_cmp_gt_i32 s56, 0
	s_mov_b64 s[14:15], -1
	s_cbranch_scc1 .LBB0_745
	s_cmp_gt_i32 s54, 0x201ff
	s_cselect_b64 s[14:15], -1, 0
	s_cmp_lt_i32 s54, 0x20200
	s_mov_b64 s[6:7], -1
	s_cbranch_scc1 .LBB0_722
	s_add_i32 s2, s54, 0xfffdfe00
	s_lshr_b32 s8, s2, 8
	s_and_b32 s10, s54, 0xe0
	s_cmp_lt_u32 s2, 0x10000
	s_cselect_b64 s[6:7], -1, 0
	s_lshl_b32 s2, s2, 10
	s_and_b32 s2, s2, 0x3fc0000
	s_and_b64 s[6:7], s[6:7], exec
	s_cselect_b32 s6, 0xc0, s78
	s_cselect_b32 s2, s2, 0
	s_add_u32 s6, s24, s6
	s_addc_u32 s7, s25, 0
	s_load_dwordx2 s[6:7], s[6:7], 0x0
	s_lshl_b32 s2, s2, 2
	s_load_dwordx2 s[18:19], s[24:25], 0x158
	s_waitcnt lgkmcnt(0)
	s_add_u32 s2, s6, s2
	s_addc_u32 s6, s7, 0
	s_lshl_b32 s7, s54, 7
	s_lshl_b32 s11, s54, 5
	s_and_b32 s7, s7, 0xf80
	s_add_u32 s16, s2, s7
	s_addc_u32 s17, s6, 0
	s_lshl_b64 s[6:7], s[8:9], 19
	s_add_u32 s18, s18, s6
	s_addc_u32 s19, s19, s7
	s_lshl_b32 s6, s54, 4
	s_and_b32 s2, s11, 0x300
	s_and_b32 s6, s6, 0x60
	s_or_b32 s2, s2, s6
	s_lshl_b32 s6, s54, 3
	s_and_b32 s6, s6, 8
	s_or_b32 s8, s2, s6
	s_mov_b64 s[6:7], 0

; DEVI f32x4 ld_nt(const float* p) { return __builtin_nontemporal_load((const f32x4*)p); }
; DEVI void cv_next(const Params& p, int l, int s, int lane, int stride, CvRun& run) {
;     ...
;     run.c = cv_slice(p, l, s, lane); run.left = 0;
;     if ((stride & 511) == 0) {
;         if (s < NS_W13) { const int e = s >> 9, es = stride >> 9; if (e < NE) { run.left = (NE - 1 - e) / es; run.sstep = (long)es * 1024 * 256; run.dstep = (long)es * 512 * 1024; } }
;         else { const int e = (s - NS_W13) >> 8, es = stride >> 8; if (e < NE) { run.left = (NE - 1 - e) / es; run.sstep = (long)es * 256 * 1024; run.dstep = (long)es * 1024 * 256; } } }
; }
; DEVI void cv_issue(const Params& p, int l, int s, int lane, CvRegs& R, CvRun& run) {
;     R.live = s < NS_SLICES ? 1 : 0;
;     if (R.live) { cv_next(p, l, s, lane, (int)gridDim.x * 8, run); R.c = run.c; const int kq = lane >> 3;
;         const float* sp = R.c.src + (size_t)(R.c.k0 + 2 * kq) * R.c.ld;
;         R.a0 = ld_nt(sp); R.b0 = ld_nt(sp + R.c.ld); R.a1 = ld_nt(sp + (size_t)16 * R.c.ld); R.b1 = ld_nt(sp + (size_t)17 * R.c.ld); }
.LBB0_744:
	v_lshlrev_b32_e32 v174, 2, v114
	v_lshl_add_u64 v[82:83], s[16:17], 0, v[174:175]
	s_mov_b64 s[68:69], s[16:17]
	s_mov_b64 s[14:15], 0
	v_mov_b64_e32 v[182:183], s[18:19]
.LBB0_745:
	s_and_b64 vcc, exec, s[14:15]
	s_cbranch_vccz .LBB0_747
	s_lshl_b64 s[6:7], s[26:27], 1
	v_lshl_add_u64 v[82:83], s[28:29], 2, v[170:171]
	s_lshl_b64 s[14:15], s[28:29], 2
	s_add_u32 s68, s68, s14
	s_addc_u32 s69, s69, s15
	v_lshl_add_u64 v[182:183], v[172:173], 0, s[6:7]
	s_add_i32 s2, s56, -1
	s_mov_b32 s8, s60
	s_mov_b32 s94, s59
	s_mov_b32 s10, s58
	s_mov_b32 s6, s57
	s_mov_b32 s95, s55
	s_mov_b64 s[22:23], s[28:29]
	s_mov_b64 s[20:21], s[26:27]
.LBB0_747:
	v_add_u32_e32 v84, s10, v128
	v_mul_lo_u32 v243, v84, s6
	v_lshlrev_b32_e32 v242, 2, v114
	s_lshl_b32 s72, s6, 2
	s_lshl_b32 s73, s6, 6
	v_lshl_add_u32 v242, v243, 2, v242
	v_add_u32_e32 v243, s72, v242
	v_add_u32_e32 v244, s73, v242
	v_add_u32_e32 v245, s73, v243
	s_ashr_i32 s7, s6, 31
	v_mad_i64_i32 v[84:85], s[14:15], v84, s6, 0
	v_lshl_add_u64 v[84:85], v[84:85], 2, v[82:83]
	s_lshl_b64 s[14:15], s[6:7], 2
	v_lshl_add_u64 v[86:87], v[84:85], 0, s[14:15]
	global_load_dwordx4 v[154:157], v[84:85], off nt
	global_load_dwordx4 v[158:161], v[86:87], off nt
	v_mad_i64_i32 v[84:85], s[16:17], s6, 60, v[86:87]
	v_lshl_add_u64 v[86:87], v[84:85], 0, s[14:15]
	global_load_dwordx4 v[162:165], v[84:85], off nt
	global_load_dwordx4 v[166:169], v[86:87], off nt
	s_mov_b64 s[26:27], s[20:21]
	s_mov_b64 s[28:29], s[22:23]
	s_mov_b32 s56, s2
	s_mov_b32 s55, s95
	v_mov_b64_e32 v[170:171], v[82:83]
	s_mov_b32 s57, s6
	s_mov_b32 s58, s10
	v_mov_b64_e32 v[172:173], v[182:183]
	s_mov_b32 s59, s94
	s_mov_b32 s60, s8

; DEVI CvSlice cv_slice(const Params& p, int l, int s, int lane) {
;     CvSlice c;
;     if (s < NS_W13) {
;         const int e = s >> 9, r = s & 511, hb = r & 7, mat = (r >> 3) & 1, ks = r >> 4;
;         const float* W = mat ? (e < NE ? p.w3 + ((size_t)l * NE + e) * 1024 * 256 : p.ws3 + (size_t)l * 1024 * 256)
;                              : (e < NE ? p.w1 + ((size_t)l * NE + e) * 1024 * 256 : p.ws1 + (size_t)l * 1024 * 256);
;         const int hc0 = hb * 32;
;         c.src = W + hc0 + (lane & 7) * 4; c.ld = 256; c.dst = p.w13t + (size_t)e * 512 * 1024; c.K = 1024;
;         c.r0 = (hc0 >> 7) * 256 + ((hc0 >> 5) & 3) * 32 + mat * 16; c.k0 = ks * 32; c.perm = 0;
;     } else {
;         s -= NS_W13;
;         const int e = s >> 8, r = s & 255, nb = r & 31, ks = r >> 5;
;         const float* W2 = e < NE ? p.w2 + ((size_t)l * NE + e) * 256 * 1024 : p.ws2 + (size_t)l * 256 * 1024;
;         c.src = W2 + nb * 32 + (lane & 7) * 4; c.ld = 1024; c.dst = p.w2t + (size_t)e * 1024 * 256; c.K = 256; c.r0 = (nb >> 3) * 256 + ((nb & 7) >> 1) * 32 + (nb & 1) * 8; c.k0 = ks * 32; c.perm = 1;
;     }
;     return c;
; }
; DEVI void cv_next(const Params& p, int l, int s, int lane, int stride, CvRun& run) {
;     ...
;     run.c = cv_slice(p, l, s, lane); run.left = 0;
;     if ((stride & 511) == 0) {
;         if (s < NS_W13) { const int e = s >> 9, es = stride >> 9; if (e < NE) { run.left = (NE - 1 - e) / es; run.sstep = (long)es * 1024 * 256; run.dstep = (long)es * 512 * 1024; } }
;         else { const int e = (s - NS_W13) >> 8, es = stride >> 8; if (e < NE) { run.left = (NE - 1 - e) / es; run.sstep = (long)es * 256 * 1024; run.dstep = (long)es * 1024 * 256; } } }
; }
; DEVI void cv_issue(const Params& p, int l, int s, int lane, CvRegs& R, CvRun& run) {
;     R.live = s < NS_SLICES ? 1 : 0;
;     if (R.live) { cv_next(p, l, s, lane, (int)gridDim.x * 8, run); R.c = run.c; const int kq = lane >> 3;
.LBB0_2282:
	v_lshlrev_b32_e32 v250, 2, v114
	v_mov_b32_e32 v251, 0
	v_lshl_add_u64 v[170:171], s[68:69], 0, v[250:251]
	s_cmp_lt_i32 s54, 0x30300
	s_cselect_b64 s[12:13], -1, 0
	s_cmp_gt_i32 s54, 0x302ff
	s_cbranch_scc1 .LBB0_2312
	s_cmp_gt_i32 s56, 0
	s_mov_b64 s[14:15], -1
	s_cbranch_scc1 .LBB0_2309
	s_cmp_gt_i32 s54, 0x201ff
	s_cselect_b64 s[14:15], -1, 0
	s_cmp_lt_i32 s54, 0x20200
	s_mov_b64 s[6:7], -1
	s_cbranch_scc1 .LBB0_2286
	s_add_i32 s2, s54, 0xfffdfe00
	s_lshr_b32 s8, s2, 8
	s_and_b32 s10, s54, 0xe0
	s_cmp_lt_u32 s2, 0x10000
	s_cselect_b64 s[6:7], -1, 0
	s_lshl_b32 s2, s2, 10
	s_and_b32 s2, s2, 0x3fc0000
	s_bitset1_b32 s2, 26
	s_and_b64 s[6:7], s[6:7], exec
	s_cselect_b32 s6, 0xc0, s79
	s_cselect_b32 s2, s2, 0x40000
	s_add_u32 s6, s24, s6
	s_addc_u32 s7, s25, 0
	s_load_dwordx2 s[6:7], s[6:7], 0x0
	s_lshl_b32 s2, s2, 2
	s_load_dwordx2 s[18:19], s[24:25], 0x158
	s_waitcnt lgkmcnt(0)
	s_add_u32 s2, s6, s2
	s_addc_u32 s6, s7, 0
	s_lshl_b32 s7, s54, 7
	s_lshl_b32 s11, s54, 5
	s_and_b32 s7, s7, 0xf80
	s_add_u32 s16, s2, s7
	s_addc_u32 s17, s6, 0
	s_lshl_b64 s[6:7], s[8:9], 19
	s_add_u32 s18, s18, s6
	s_addc_u32 s19, s19, s7
	s_lshl_b32 s6, s54, 4
	s_and_b32 s2, s11, 0x300
	s_and_b32 s6, s6, 0x60
	s_or_b32 s2, s2, s6
	s_lshl_b32 s6, s54, 3
	s_and_b32 s6, s6, 8
	s_or_b32 s8, s2, s6
	s_mov_b64 s[6:7], 0
